# P9 routing top-8 loop: wave max via 2 DPP row_bcast hops + 1 readlane instead of 4 readlanes + 5 VALU (16 sites)
# baseline (speedup 1.0000x reference)
; template <int CTRL> __device__ __forceinline__ float dppf(float x) { return __builtin_bit_cast(float, __builtin_amdgcn_update_dpp(0, __builtin_bit_cast(int, x), CTRL, 0xF, 0xF, true)); }
; __device__ __forceinline__ void p9_fused4(Frame& F) {
;     ...
;         for (int q = 0; q < 2; ++q) {
;             const int rp_ = 0; const int tl = wave * 2 + q, t = t0 + pass * 16 + tl;
;             const float logit = lg[tl * 64 + lane];
;             const float score = 1.f / (1.f + __expf(-logit)), choice = score + rb;
;             float m1 = choice; m1 = fmaxf(m1, dppf<0xB1>(m1)); m1 = fmaxf(m1, dppf<0x4E>(m1)); m1 = fmaxf(m1, dppf<0x141>(m1));
.LBB0_1405:
	v_add_u32_e32 v146, s37, v191
	s_waitcnt lgkmcnt(0)
	s_barrier
	ds_read_b32 v146, v146
	s_waitcnt lgkmcnt(0)
	v_mul_f32_e32 v146, 0xbfb8aa3b, v146
	v_exp_f32_e32 v146, v146
	s_nop 0
	v_add_f32_e32 v146, 1.0, v146
	v_div_scale_f32 v147, s[22:23], v146, v146, 1.0
	v_rcp_f32_e32 v148, v147
	v_div_scale_f32 v149, vcc, 1.0, v146, 1.0
	v_fma_f32 v150, -v147, v148, 1.0
	v_fmac_f32_e32 v148, v150, v148
	v_mul_f32_e32 v150, v149, v148
	v_fma_f32 v151, -v147, v150, v149
	v_fmac_f32_e32 v150, v151, v148
	v_fma_f32 v147, -v147, v150, v149
	v_div_fmas_f32 v147, v147, v148, v150
	v_div_fixup_f32 v146, v147, v146, 1.0
	v_add_f32_e32 v147, v182, v146
	s_nop 1
	v_max_f32_dpp v148, v147, v147 quad_perm:[1,0,3,2] row_mask:0xf bank_mask:0xf bound_ctrl:1


; template <int CTRL> __device__ __forceinline__ float dppf(float x) { return __builtin_bit_cast(float, __builtin_amdgcn_update_dpp(0, __builtin_bit_cast(int, x), CTRL, 0xF, 0xF, true)); }
; __device__ __forceinline__ void p9_fused4(Frame& F) {
;     ...
;             float m1 = choice; m1 = fmaxf(m1, dppf<0xB1>(m1)); m1 = fmaxf(m1, dppf<0x4E>(m1)); m1 = fmaxf(m1, dppf<0x141>(m1));
	s_nop 1
	v_max_f32_dpp v148, v148, v148 quad_perm:[2,3,0,1] row_mask:0xf bank_mask:0xf bound_ctrl:1


; template <int CTRL> __device__ __forceinline__ float dppf(float x) { return __builtin_bit_cast(float, __builtin_amdgcn_update_dpp(0, __builtin_bit_cast(int, x), CTRL, 0xF, 0xF, true)); }
; __device__ __forceinline__ void p9_fused4(Frame& F) {
;     ...
;             float m1 = choice; m1 = fmaxf(m1, dppf<0xB1>(m1)); m1 = fmaxf(m1, dppf<0x4E>(m1)); m1 = fmaxf(m1, dppf<0x141>(m1));
	s_nop 1
	v_max_f32_dpp v148, v148, v148 row_half_mirror row_mask:0xf bank_mask:0xf bound_ctrl:1


; template <int CTRL> __device__ __forceinline__ float dppf(float x) { return __builtin_bit_cast(float, __builtin_amdgcn_update_dpp(0, __builtin_bit_cast(int, x), CTRL, 0xF, 0xF, true)); }
; template <int CTRL> __device__ __forceinline__ int dppi(int x) { return __builtin_amdgcn_update_dpp(0, x, CTRL, 0xF, 0xF, true); }
; __device__ __forceinline__ void p9_fused4(Frame& F) {
;     ...
;             int cand = (choice == m1) ? (lane & 7) : 8; cand = min(cand, dppi<0xB1>(cand)); cand = min(cand, dppi<0x4E>(cand)); cand = min(cand, dppi<0x141>(cand));
;             float m2 = ((lane & 7) == cand) ? -__builtin_inff() : choice; m2 = fmaxf(m2, dppf<0xB1>(m2)); m2 = fmaxf(m2, dppf<0x4E>(m2)); m2 = fmaxf(m2, dppf<0x141>(m2));
	v_cmp_eq_f32_e32 vcc, v147, v148
	s_nop 1
	v_cndmask_b32_e32 v149, 8, v192, vcc
	s_nop 1
	v_min_i32_dpp v149, v149, v149 quad_perm:[1,0,3,2] row_mask:0xf bank_mask:0xf bound_ctrl:1
	s_nop 1
	v_min_i32_dpp v149, v149, v149 quad_perm:[2,3,0,1] row_mask:0xf bank_mask:0xf bound_ctrl:1
	s_nop 1
	v_min_i32_dpp v149, v149, v149 row_half_mirror row_mask:0xf bank_mask:0xf bound_ctrl:1
	v_cmp_ne_u32_e32 vcc, v192, v149
	s_nop 1
	v_cndmask_b32_e32 v149, v211, v147, vcc
	s_nop 1
	v_max_f32_dpp v149, v149, v149 quad_perm:[1,0,3,2] row_mask:0xf bank_mask:0xf bound_ctrl:1


; template <int CTRL> __device__ __forceinline__ float dppf(float x) { return __builtin_bit_cast(float, __builtin_amdgcn_update_dpp(0, __builtin_bit_cast(int, x), CTRL, 0xF, 0xF, true)); }
; __device__ __forceinline__ void p9_fused4(Frame& F) {
;     ...
;             float m2 = ((lane & 7) == cand) ? -__builtin_inff() : choice; m2 = fmaxf(m2, dppf<0xB1>(m2)); m2 = fmaxf(m2, dppf<0x4E>(m2)); m2 = fmaxf(m2, dppf<0x141>(m2));
	s_nop 1
	v_max_f32_dpp v149, v149, v149 quad_perm:[2,3,0,1] row_mask:0xf bank_mask:0xf bound_ctrl:1


; template <int CTRL> __device__ __forceinline__ float dppf(float x) { return __builtin_bit_cast(float, __builtin_amdgcn_update_dpp(0, __builtin_bit_cast(int, x), CTRL, 0xF, 0xF, true)); }
; __device__ __forceinline__ void p9_fused4(Frame& F) {
;     ...
;             float m2 = ((lane & 7) == cand) ? -__builtin_inff() : choice; m2 = fmaxf(m2, dppf<0xB1>(m2)); m2 = fmaxf(m2, dppf<0x4E>(m2)); m2 = fmaxf(m2, dppf<0x141>(m2));
	s_nop 1
	v_max_f32_dpp v149, v149, v149 row_half_mirror row_mask:0xf bank_mask:0xf bound_ctrl:1


; template <int CTRL> __device__ __forceinline__ float dppf(float x) { return __builtin_bit_cast(float, __builtin_amdgcn_update_dpp(0, __builtin_bit_cast(int, x), CTRL, 0xF, 0xF, true)); }
; __device__ __forceinline__ void p9_fused4(Frame& F) {
;     ...
;             const float gs = m1 + m2; const int g = lane >> 3; int rank = 0;
; #pragma unroll
;             for (int gg = 0; gg < 8; ++gg) { const float sgg = __builtin_bit_cast(float, __builtin_amdgcn_readlane(__builtin_bit_cast(int, gs), gg * 8)); rank += (sgg > gs || (sgg == gs && gg < g)) ? 1 : 0; }
;             const float masked = (rank < 4) ? choice : -1e30f;
;             float v = masked, ssum = 0.f; int r = 8;
; #pragma unroll
;             for (int kk = 0; kk < 8; ++kk) {
;                 float m = v; m = fmaxf(m, dppf<0xB1>(m)); m = fmaxf(m, dppf<0x4E>(m)); m = fmaxf(m, dppf<0x141>(m)); m = fmaxf(m, dppf<0x140>(m));
	v_add_f32_e32 v148, v148, v149
	s_nop 0
	v_readlane_b32 s22, v148, 0
	s_nop 1
	v_cmp_gt_f32_e32 vcc, s22, v148
	v_cmp_eq_f32_e64 s[22:23], s22, v148
	s_and_b64 s[22:23], s[22:23], s[6:7]
	s_or_b64 s[22:23], vcc, s[22:23]
	v_cndmask_b32_e64 v149, 0, 1, s[22:23]
	v_readlane_b32 s22, v148, 8
	s_nop 1
	v_cmp_gt_f32_e32 vcc, s22, v148
	v_cmp_eq_f32_e64 s[22:23], s22, v148
	s_and_b64 s[22:23], s[22:23], s[8:9]
	s_or_b64 s[22:23], vcc, s[22:23]
	v_cndmask_b32_e64 v150, 0, 1, s[22:23]
	v_readlane_b32 s22, v148, 16
	s_nop 1
	v_cmp_gt_f32_e32 vcc, s22, v148
	v_cmp_eq_f32_e64 s[22:23], s22, v148
	s_and_b64 s[22:23], s[22:23], s[10:11]
	s_or_b64 s[22:23], vcc, s[22:23]
	v_cndmask_b32_e64 v151, 0, 1, s[22:23]
	v_readlane_b32 s22, v148, 24
	s_nop 1
	v_cmp_gt_f32_e32 vcc, s22, v148
	v_cmp_eq_f32_e64 s[22:23], s22, v148
	s_and_b64 s[22:23], s[22:23], s[12:13]
	s_or_b64 s[22:23], vcc, s[22:23]
	v_cndmask_b32_e64 v152, 0, 1, s[22:23]
	v_readlane_b32 s22, v148, 32
	s_nop 1
	v_cmp_gt_f32_e32 vcc, s22, v148
	v_cmp_eq_f32_e64 s[22:23], s22, v148
	s_and_b64 s[22:23], s[22:23], s[14:15]
	s_or_b64 s[22:23], vcc, s[22:23]
	v_cndmask_b32_e64 v153, 0, 1, s[22:23]
	v_readlane_b32 s22, v148, 40
	s_nop 1
	v_cmp_gt_f32_e32 vcc, s22, v148
	v_cmp_eq_f32_e64 s[22:23], s22, v148
	s_and_b64 s[22:23], s[22:23], s[16:17]
	s_or_b64 s[22:23], vcc, s[22:23]
	v_cndmask_b32_e64 v154, 0, 1, s[22:23]
	v_readlane_b32 s22, v148, 48
	s_nop 1
	v_cmp_gt_f32_e32 vcc, s22, v148
	v_cmp_eq_f32_e64 s[22:23], s22, v148
	s_and_b64 s[22:23], s[18:19], s[22:23]
	s_or_b64 s[22:23], vcc, s[22:23]
	v_cndmask_b32_e64 v155, 0, 1, s[22:23]
	v_readlane_b32 s22, v148, 56
	s_nop 1
	v_cmp_gt_f32_e32 vcc, s22, v148
	s_nop 1
	v_cndmask_b32_e64 v148, 0, 1, vcc
	v_add_u32_e32 v148, v150, v148
	v_add3_u32 v148, v148, v149, v151
	v_add3_u32 v148, v148, v152, v153
	v_add3_u32 v148, v148, v154, v155
	v_cmp_gt_u32_e32 vcc, 4, v148
	s_nop 1
	v_cndmask_b32_e32 v147, v212, v147, vcc
	s_nop 1
	v_max_f32_dpp v148, v147, v147 quad_perm:[1,0,3,2] row_mask:0xf bank_mask:0xf bound_ctrl:1


; template <int CTRL> __device__ __forceinline__ float dppf(float x) { return __builtin_bit_cast(float, __builtin_amdgcn_update_dpp(0, __builtin_bit_cast(int, x), CTRL, 0xF, 0xF, true)); }
; __device__ __forceinline__ void p9_fused4(Frame& F) {
;     ...
;                 float m = v; m = fmaxf(m, dppf<0xB1>(m)); m = fmaxf(m, dppf<0x4E>(m)); m = fmaxf(m, dppf<0x141>(m)); m = fmaxf(m, dppf<0x140>(m));
	s_nop 1
	v_max_f32_dpp v148, v148, v148 quad_perm:[2,3,0,1] row_mask:0xf bank_mask:0xf bound_ctrl:1


; template <int CTRL> __device__ __forceinline__ float dppf(float x) { return __builtin_bit_cast(float, __builtin_amdgcn_update_dpp(0, __builtin_bit_cast(int, x), CTRL, 0xF, 0xF, true)); }
; __device__ __forceinline__ void p9_fused4(Frame& F) {
;     ...
;                 float m = v; m = fmaxf(m, dppf<0xB1>(m)); m = fmaxf(m, dppf<0x4E>(m)); m = fmaxf(m, dppf<0x141>(m)); m = fmaxf(m, dppf<0x140>(m));
	s_nop 1
	v_max_f32_dpp v148, v148, v148 row_half_mirror row_mask:0xf bank_mask:0xf bound_ctrl:1


; template <int CTRL> __device__ __forceinline__ float dppf(float x) { return __builtin_bit_cast(float, __builtin_amdgcn_update_dpp(0, __builtin_bit_cast(int, x), CTRL, 0xF, 0xF, true)); }
; __device__ __forceinline__ void p9_fused4(Frame& F) {
;     ...
;                 float m = v; m = fmaxf(m, dppf<0xB1>(m)); m = fmaxf(m, dppf<0x4E>(m)); m = fmaxf(m, dppf<0x141>(m)); m = fmaxf(m, dppf<0x140>(m));
	s_nop 1
	v_max_f32_dpp v148, v148, v148 row_mirror row_mask:0xf bank_mask:0xf bound_ctrl:1


; template <int CTRL> __device__ __forceinline__ float dppf(float x) { return __builtin_bit_cast(float, __builtin_amdgcn_update_dpp(0, __builtin_bit_cast(int, x), CTRL, 0xF, 0xF, true)); }
; __device__ __forceinline__ void p9_fused4(Frame& F) {
;     ...
;                 float m = v; m = fmaxf(m, dppf<0xB1>(m)); m = fmaxf(m, dppf<0x4E>(m)); m = fmaxf(m, dppf<0x141>(m)); m = fmaxf(m, dppf<0x140>(m));
;                 const float r0 = __builtin_bit_cast(float, __builtin_amdgcn_readlane(__builtin_bit_cast(int, m), 0)), r1 = __builtin_bit_cast(float, __builtin_amdgcn_readlane(__builtin_bit_cast(int, m), 16));
;                 const float r2 = __builtin_bit_cast(float, __builtin_amdgcn_readlane(__builtin_bit_cast(int, m), 32)), r3 = __builtin_bit_cast(float, __builtin_amdgcn_readlane(__builtin_bit_cast(int, m), 48));
;                 const float wm = fmaxf(fmaxf(r0, r1), fmaxf(r2, r3));
;                 const unsigned long long bal = __builtin_amdgcn_ballot_w64(v == wm);
;                 const int selL = (int)__builtin_ctzll(bal);
;                 ssum += __builtin_bit_cast(float, __builtin_amdgcn_readlane(__builtin_bit_cast(int, score), selL));
;                 if (lane == selL) { r = kk; v = -__builtin_inff(); }
	s_nop 1
	v_max_f32_dpp v148, v148, v148 row_bcast:15 row_mask:0xa bank_mask:0xf
	s_nop 1
	v_max_f32_dpp v148, v148, v148 row_bcast:31 row_mask:0xc bank_mask:0xf
	s_nop 0
	v_readlane_b32 s22, v148, 63
	s_nop 1
	v_cmp_eq_f32_e32 vcc, s22, v147
	s_ff1_i32_b64 s22, vcc
	v_cmp_eq_u32_e32 vcc, s22, v163
	v_readlane_b32 s56, v146, s22
	s_nop 0
	v_cndmask_b32_e32 v147, v147, v211, vcc
	v_cndmask_b32_e64 v148, 8, 0, vcc
	s_nop 0
	v_max_f32_dpp v149, v147, v147 quad_perm:[1,0,3,2] row_mask:0xf bank_mask:0xf bound_ctrl:1


; template <int CTRL> __device__ __forceinline__ float dppf(float x) { return __builtin_bit_cast(float, __builtin_amdgcn_update_dpp(0, __builtin_bit_cast(int, x), CTRL, 0xF, 0xF, true)); }
; __device__ __forceinline__ void p9_fused4(Frame& F) {
;     ...
;                 float m = v; m = fmaxf(m, dppf<0xB1>(m)); m = fmaxf(m, dppf<0x4E>(m)); m = fmaxf(m, dppf<0x141>(m)); m = fmaxf(m, dppf<0x140>(m));
	s_nop 1
	v_max_f32_dpp v149, v149, v149 quad_perm:[2,3,0,1] row_mask:0xf bank_mask:0xf bound_ctrl:1


; template <int CTRL> __device__ __forceinline__ float dppf(float x) { return __builtin_bit_cast(float, __builtin_amdgcn_update_dpp(0, __builtin_bit_cast(int, x), CTRL, 0xF, 0xF, true)); }
; __device__ __forceinline__ void p9_fused4(Frame& F) {
;     ...
;                 float m = v; m = fmaxf(m, dppf<0xB1>(m)); m = fmaxf(m, dppf<0x4E>(m)); m = fmaxf(m, dppf<0x141>(m)); m = fmaxf(m, dppf<0x140>(m));
	s_nop 1
	v_max_f32_dpp v149, v149, v149 row_half_mirror row_mask:0xf bank_mask:0xf bound_ctrl:1


; template <int CTRL> __device__ __forceinline__ float dppf(float x) { return __builtin_bit_cast(float, __builtin_amdgcn_update_dpp(0, __builtin_bit_cast(int, x), CTRL, 0xF, 0xF, true)); }
; __device__ __forceinline__ void p9_fused4(Frame& F) {
;     ...
;                 float m = v; m = fmaxf(m, dppf<0xB1>(m)); m = fmaxf(m, dppf<0x4E>(m)); m = fmaxf(m, dppf<0x141>(m)); m = fmaxf(m, dppf<0x140>(m));
	s_nop 1
	v_max_f32_dpp v149, v149, v149 row_mirror row_mask:0xf bank_mask:0xf bound_ctrl:1


; template <int CTRL> __device__ __forceinline__ float dppf(float x) { return __builtin_bit_cast(float, __builtin_amdgcn_update_dpp(0, __builtin_bit_cast(int, x), CTRL, 0xF, 0xF, true)); }
; __device__ __forceinline__ void p9_fused4(Frame& F) {
;     ...
;                 float m = v; m = fmaxf(m, dppf<0xB1>(m)); m = fmaxf(m, dppf<0x4E>(m)); m = fmaxf(m, dppf<0x141>(m)); m = fmaxf(m, dppf<0x140>(m));
;                 const float r0 = __builtin_bit_cast(float, __builtin_amdgcn_readlane(__builtin_bit_cast(int, m), 0)), r1 = __builtin_bit_cast(float, __builtin_amdgcn_readlane(__builtin_bit_cast(int, m), 16));
;                 const float r2 = __builtin_bit_cast(float, __builtin_amdgcn_readlane(__builtin_bit_cast(int, m), 32)), r3 = __builtin_bit_cast(float, __builtin_amdgcn_readlane(__builtin_bit_cast(int, m), 48));
;                 const float wm = fmaxf(fmaxf(r0, r1), fmaxf(r2, r3));
;                 const unsigned long long bal = __builtin_amdgcn_ballot_w64(v == wm);
;                 const int selL = (int)__builtin_ctzll(bal);
;                 ssum += __builtin_bit_cast(float, __builtin_amdgcn_readlane(__builtin_bit_cast(int, score), selL));
;                 if (lane == selL) { r = kk; v = -__builtin_inff(); }
	s_nop 1
	v_max_f32_dpp v149, v149, v149 row_bcast:15 row_mask:0xa bank_mask:0xf
	s_nop 1
	v_max_f32_dpp v149, v149, v149 row_bcast:31 row_mask:0xc bank_mask:0xf
	s_nop 0
	v_readlane_b32 s22, v149, 63
	s_nop 1
	v_cmp_eq_f32_e32 vcc, s22, v147
	s_ff1_i32_b64 s22, vcc
	v_cmp_eq_u32_e32 vcc, s22, v163
	v_readlane_b32 s57, v146, s22
	s_nop 0
	v_cndmask_b32_e32 v147, v147, v211, vcc
	v_cndmask_b32_e64 v148, v148, 1, vcc
	s_nop 0
	v_max_f32_dpp v149, v147, v147 quad_perm:[1,0,3,2] row_mask:0xf bank_mask:0xf bound_ctrl:1


; template <int CTRL> __device__ __forceinline__ float dppf(float x) { return __builtin_bit_cast(float, __builtin_amdgcn_update_dpp(0, __builtin_bit_cast(int, x), CTRL, 0xF, 0xF, true)); }
; __device__ __forceinline__ void p9_fused4(Frame& F) {
;     ...
;                 float m = v; m = fmaxf(m, dppf<0xB1>(m)); m = fmaxf(m, dppf<0x4E>(m)); m = fmaxf(m, dppf<0x141>(m)); m = fmaxf(m, dppf<0x140>(m));
	s_nop 1
	v_max_f32_dpp v149, v149, v149 quad_perm:[2,3,0,1] row_mask:0xf bank_mask:0xf bound_ctrl:1


; template <int CTRL> __device__ __forceinline__ float dppf(float x) { return __builtin_bit_cast(float, __builtin_amdgcn_update_dpp(0, __builtin_bit_cast(int, x), CTRL, 0xF, 0xF, true)); }
; __device__ __forceinline__ void p9_fused4(Frame& F) {
;     ...
;                 float m = v; m = fmaxf(m, dppf<0xB1>(m)); m = fmaxf(m, dppf<0x4E>(m)); m = fmaxf(m, dppf<0x141>(m)); m = fmaxf(m, dppf<0x140>(m));
	s_nop 1
	v_max_f32_dpp v149, v149, v149 row_half_mirror row_mask:0xf bank_mask:0xf bound_ctrl:1


; template <int CTRL> __device__ __forceinline__ float dppf(float x) { return __builtin_bit_cast(float, __builtin_amdgcn_update_dpp(0, __builtin_bit_cast(int, x), CTRL, 0xF, 0xF, true)); }
; __device__ __forceinline__ void p9_fused4(Frame& F) {
;     ...
;                 float m = v; m = fmaxf(m, dppf<0xB1>(m)); m = fmaxf(m, dppf<0x4E>(m)); m = fmaxf(m, dppf<0x141>(m)); m = fmaxf(m, dppf<0x140>(m));
	s_nop 1
	v_max_f32_dpp v149, v149, v149 row_mirror row_mask:0xf bank_mask:0xf bound_ctrl:1


; template <int CTRL> __device__ __forceinline__ float dppf(float x) { return __builtin_bit_cast(float, __builtin_amdgcn_update_dpp(0, __builtin_bit_cast(int, x), CTRL, 0xF, 0xF, true)); }
; __device__ __forceinline__ void p9_fused4(Frame& F) {
;     ...
;                 float m = v; m = fmaxf(m, dppf<0xB1>(m)); m = fmaxf(m, dppf<0x4E>(m)); m = fmaxf(m, dppf<0x141>(m)); m = fmaxf(m, dppf<0x140>(m));
;                 const float r0 = __builtin_bit_cast(float, __builtin_amdgcn_readlane(__builtin_bit_cast(int, m), 0)), r1 = __builtin_bit_cast(float, __builtin_amdgcn_readlane(__builtin_bit_cast(int, m), 16));
;                 const float r2 = __builtin_bit_cast(float, __builtin_amdgcn_readlane(__builtin_bit_cast(int, m), 32)), r3 = __builtin_bit_cast(float, __builtin_amdgcn_readlane(__builtin_bit_cast(int, m), 48));
;                 const float wm = fmaxf(fmaxf(r0, r1), fmaxf(r2, r3));
;                 const unsigned long long bal = __builtin_amdgcn_ballot_w64(v == wm);
;                 const int selL = (int)__builtin_ctzll(bal);
;                 ssum += __builtin_bit_cast(float, __builtin_amdgcn_readlane(__builtin_bit_cast(int, score), selL));
;                 if (lane == selL) { r = kk; v = -__builtin_inff(); }
	s_nop 1
	v_max_f32_dpp v149, v149, v149 row_bcast:15 row_mask:0xa bank_mask:0xf
	s_nop 1
	v_max_f32_dpp v149, v149, v149 row_bcast:31 row_mask:0xc bank_mask:0xf
	s_nop 0
	v_readlane_b32 s22, v149, 63
	s_nop 1
	v_cmp_eq_f32_e32 vcc, s22, v147
	s_ff1_i32_b64 s22, vcc
	v_cmp_eq_u32_e32 vcc, s22, v163
	v_readlane_b32 s58, v146, s22
	s_nop 0
	v_cndmask_b32_e32 v147, v147, v211, vcc
	v_cndmask_b32_e64 v148, v148, 2, vcc
	s_nop 0
	v_max_f32_dpp v149, v147, v147 quad_perm:[1,0,3,2] row_mask:0xf bank_mask:0xf bound_ctrl:1


; template <int CTRL> __device__ __forceinline__ float dppf(float x) { return __builtin_bit_cast(float, __builtin_amdgcn_update_dpp(0, __builtin_bit_cast(int, x), CTRL, 0xF, 0xF, true)); }
; __device__ __forceinline__ void p9_fused4(Frame& F) {
;     ...
;                 float m = v; m = fmaxf(m, dppf<0xB1>(m)); m = fmaxf(m, dppf<0x4E>(m)); m = fmaxf(m, dppf<0x141>(m)); m = fmaxf(m, dppf<0x140>(m));
	s_nop 1
	v_max_f32_dpp v149, v149, v149 quad_perm:[2,3,0,1] row_mask:0xf bank_mask:0xf bound_ctrl:1


; template <int CTRL> __device__ __forceinline__ float dppf(float x) { return __builtin_bit_cast(float, __builtin_amdgcn_update_dpp(0, __builtin_bit_cast(int, x), CTRL, 0xF, 0xF, true)); }
; __device__ __forceinline__ void p9_fused4(Frame& F) {
;     ...
;                 float m = v; m = fmaxf(m, dppf<0xB1>(m)); m = fmaxf(m, dppf<0x4E>(m)); m = fmaxf(m, dppf<0x141>(m)); m = fmaxf(m, dppf<0x140>(m));
	s_nop 1
	v_max_f32_dpp v149, v149, v149 row_half_mirror row_mask:0xf bank_mask:0xf bound_ctrl:1


; template <int CTRL> __device__ __forceinline__ float dppf(float x) { return __builtin_bit_cast(float, __builtin_amdgcn_update_dpp(0, __builtin_bit_cast(int, x), CTRL, 0xF, 0xF, true)); }
; __device__ __forceinline__ void p9_fused4(Frame& F) {
;     ...
;                 float m = v; m = fmaxf(m, dppf<0xB1>(m)); m = fmaxf(m, dppf<0x4E>(m)); m = fmaxf(m, dppf<0x141>(m)); m = fmaxf(m, dppf<0x140>(m));
	s_nop 1
	v_max_f32_dpp v149, v149, v149 row_mirror row_mask:0xf bank_mask:0xf bound_ctrl:1


; template <int CTRL> __device__ __forceinline__ float dppf(float x) { return __builtin_bit_cast(float, __builtin_amdgcn_update_dpp(0, __builtin_bit_cast(int, x), CTRL, 0xF, 0xF, true)); }
; __device__ __forceinline__ void p9_fused4(Frame& F) {
;     ...
;                 float m = v; m = fmaxf(m, dppf<0xB1>(m)); m = fmaxf(m, dppf<0x4E>(m)); m = fmaxf(m, dppf<0x141>(m)); m = fmaxf(m, dppf<0x140>(m));
;                 const float r0 = __builtin_bit_cast(float, __builtin_amdgcn_readlane(__builtin_bit_cast(int, m), 0)), r1 = __builtin_bit_cast(float, __builtin_amdgcn_readlane(__builtin_bit_cast(int, m), 16));
;                 const float r2 = __builtin_bit_cast(float, __builtin_amdgcn_readlane(__builtin_bit_cast(int, m), 32)), r3 = __builtin_bit_cast(float, __builtin_amdgcn_readlane(__builtin_bit_cast(int, m), 48));
;                 const float wm = fmaxf(fmaxf(r0, r1), fmaxf(r2, r3));
;                 const unsigned long long bal = __builtin_amdgcn_ballot_w64(v == wm);
;                 const int selL = (int)__builtin_ctzll(bal);
;                 ssum += __builtin_bit_cast(float, __builtin_amdgcn_readlane(__builtin_bit_cast(int, score), selL));
;                 if (lane == selL) { r = kk; v = -__builtin_inff(); }
	s_nop 1
	v_max_f32_dpp v149, v149, v149 row_bcast:15 row_mask:0xa bank_mask:0xf
	s_nop 1
	v_max_f32_dpp v149, v149, v149 row_bcast:31 row_mask:0xc bank_mask:0xf
	s_nop 0
	v_readlane_b32 s22, v149, 63
	s_nop 1
	v_cmp_eq_f32_e32 vcc, s22, v147
	s_ff1_i32_b64 s22, vcc
	v_cmp_eq_u32_e32 vcc, s22, v163
	v_readlane_b32 s59, v146, s22
	s_nop 0
	v_cndmask_b32_e32 v147, v147, v211, vcc
	v_cndmask_b32_e64 v148, v148, 3, vcc
	s_nop 0
	v_max_f32_dpp v149, v147, v147 quad_perm:[1,0,3,2] row_mask:0xf bank_mask:0xf bound_ctrl:1


; template <int CTRL> __device__ __forceinline__ float dppf(float x) { return __builtin_bit_cast(float, __builtin_amdgcn_update_dpp(0, __builtin_bit_cast(int, x), CTRL, 0xF, 0xF, true)); }
; __device__ __forceinline__ void p9_fused4(Frame& F) {
;     ...
;                 float m = v; m = fmaxf(m, dppf<0xB1>(m)); m = fmaxf(m, dppf<0x4E>(m)); m = fmaxf(m, dppf<0x141>(m)); m = fmaxf(m, dppf<0x140>(m));
	s_nop 1
	v_max_f32_dpp v149, v149, v149 quad_perm:[2,3,0,1] row_mask:0xf bank_mask:0xf bound_ctrl:1


; template <int CTRL> __device__ __forceinline__ float dppf(float x) { return __builtin_bit_cast(float, __builtin_amdgcn_update_dpp(0, __builtin_bit_cast(int, x), CTRL, 0xF, 0xF, true)); }
; __device__ __forceinline__ void p9_fused4(Frame& F) {
;     ...
;                 float m = v; m = fmaxf(m, dppf<0xB1>(m)); m = fmaxf(m, dppf<0x4E>(m)); m = fmaxf(m, dppf<0x141>(m)); m = fmaxf(m, dppf<0x140>(m));
	s_nop 1
	v_max_f32_dpp v149, v149, v149 row_half_mirror row_mask:0xf bank_mask:0xf bound_ctrl:1


; template <int CTRL> __device__ __forceinline__ float dppf(float x) { return __builtin_bit_cast(float, __builtin_amdgcn_update_dpp(0, __builtin_bit_cast(int, x), CTRL, 0xF, 0xF, true)); }
; __device__ __forceinline__ void p9_fused4(Frame& F) {
;     ...
;                 float m = v; m = fmaxf(m, dppf<0xB1>(m)); m = fmaxf(m, dppf<0x4E>(m)); m = fmaxf(m, dppf<0x141>(m)); m = fmaxf(m, dppf<0x140>(m));
	s_nop 1
	v_max_f32_dpp v149, v149, v149 row_mirror row_mask:0xf bank_mask:0xf bound_ctrl:1


; template <int CTRL> __device__ __forceinline__ float dppf(float x) { return __builtin_bit_cast(float, __builtin_amdgcn_update_dpp(0, __builtin_bit_cast(int, x), CTRL, 0xF, 0xF, true)); }
; __device__ __forceinline__ void p9_fused4(Frame& F) {
;     ...
;                 float m = v; m = fmaxf(m, dppf<0xB1>(m)); m = fmaxf(m, dppf<0x4E>(m)); m = fmaxf(m, dppf<0x141>(m)); m = fmaxf(m, dppf<0x140>(m));
;                 const float r0 = __builtin_bit_cast(float, __builtin_amdgcn_readlane(__builtin_bit_cast(int, m), 0)), r1 = __builtin_bit_cast(float, __builtin_amdgcn_readlane(__builtin_bit_cast(int, m), 16));
;                 const float r2 = __builtin_bit_cast(float, __builtin_amdgcn_readlane(__builtin_bit_cast(int, m), 32)), r3 = __builtin_bit_cast(float, __builtin_amdgcn_readlane(__builtin_bit_cast(int, m), 48));
;                 const float wm = fmaxf(fmaxf(r0, r1), fmaxf(r2, r3));
;                 const unsigned long long bal = __builtin_amdgcn_ballot_w64(v == wm);
;                 const int selL = (int)__builtin_ctzll(bal);
;                 ssum += __builtin_bit_cast(float, __builtin_amdgcn_readlane(__builtin_bit_cast(int, score), selL));
;                 if (lane == selL) { r = kk; v = -__builtin_inff(); }
	s_nop 1
	v_max_f32_dpp v149, v149, v149 row_bcast:15 row_mask:0xa bank_mask:0xf
	s_nop 1
	v_max_f32_dpp v149, v149, v149 row_bcast:31 row_mask:0xc bank_mask:0xf
	s_nop 0
	v_readlane_b32 s22, v149, 63
	s_nop 1
	v_cmp_eq_f32_e32 vcc, s22, v147
	s_ff1_i32_b64 s22, vcc
	v_cmp_eq_u32_e32 vcc, s22, v163
	v_readlane_b32 s60, v146, s22
	s_nop 0
	v_cndmask_b32_e32 v147, v147, v211, vcc
	v_max_f32_e32 v150, v147, v147
	v_cndmask_b32_e64 v148, v148, 4, vcc
	v_max_f32_dpp v149, v147, v150 quad_perm:[1,0,3,2] row_mask:0xf bank_mask:0xf bound_ctrl:1


; template <int CTRL> __device__ __forceinline__ float dppf(float x) { return __builtin_bit_cast(float, __builtin_amdgcn_update_dpp(0, __builtin_bit_cast(int, x), CTRL, 0xF, 0xF, true)); }
; __device__ __forceinline__ void p9_fused4(Frame& F) {
;     ...
;                 float m = v; m = fmaxf(m, dppf<0xB1>(m)); m = fmaxf(m, dppf<0x4E>(m)); m = fmaxf(m, dppf<0x141>(m)); m = fmaxf(m, dppf<0x140>(m));
	s_nop 1
	v_max_f32_dpp v149, v149, v149 quad_perm:[2,3,0,1] row_mask:0xf bank_mask:0xf bound_ctrl:1


; template <int CTRL> __device__ __forceinline__ float dppf(float x) { return __builtin_bit_cast(float, __builtin_amdgcn_update_dpp(0, __builtin_bit_cast(int, x), CTRL, 0xF, 0xF, true)); }
; __device__ __forceinline__ void p9_fused4(Frame& F) {
;     ...
;                 float m = v; m = fmaxf(m, dppf<0xB1>(m)); m = fmaxf(m, dppf<0x4E>(m)); m = fmaxf(m, dppf<0x141>(m)); m = fmaxf(m, dppf<0x140>(m));
	s_nop 1
	v_max_f32_dpp v149, v149, v149 row_half_mirror row_mask:0xf bank_mask:0xf bound_ctrl:1


; template <int CTRL> __device__ __forceinline__ float dppf(float x) { return __builtin_bit_cast(float, __builtin_amdgcn_update_dpp(0, __builtin_bit_cast(int, x), CTRL, 0xF, 0xF, true)); }
; __device__ __forceinline__ void p9_fused4(Frame& F) {
;     ...
;                 float m = v; m = fmaxf(m, dppf<0xB1>(m)); m = fmaxf(m, dppf<0x4E>(m)); m = fmaxf(m, dppf<0x141>(m)); m = fmaxf(m, dppf<0x140>(m));
	s_nop 1
	v_max_f32_dpp v149, v149, v149 row_mirror row_mask:0xf bank_mask:0xf bound_ctrl:1


; template <int CTRL> __device__ __forceinline__ float dppf(float x) { return __builtin_bit_cast(float, __builtin_amdgcn_update_dpp(0, __builtin_bit_cast(int, x), CTRL, 0xF, 0xF, true)); }
; __device__ __forceinline__ void p9_fused4(Frame& F) {
;     ...
;                 float m = v; m = fmaxf(m, dppf<0xB1>(m)); m = fmaxf(m, dppf<0x4E>(m)); m = fmaxf(m, dppf<0x141>(m)); m = fmaxf(m, dppf<0x140>(m));
;                 const float r0 = __builtin_bit_cast(float, __builtin_amdgcn_readlane(__builtin_bit_cast(int, m), 0)), r1 = __builtin_bit_cast(float, __builtin_amdgcn_readlane(__builtin_bit_cast(int, m), 16));
;                 const float r2 = __builtin_bit_cast(float, __builtin_amdgcn_readlane(__builtin_bit_cast(int, m), 32)), r3 = __builtin_bit_cast(float, __builtin_amdgcn_readlane(__builtin_bit_cast(int, m), 48));
;                 const float wm = fmaxf(fmaxf(r0, r1), fmaxf(r2, r3));
;                 const unsigned long long bal = __builtin_amdgcn_ballot_w64(v == wm);
;                 const int selL = (int)__builtin_ctzll(bal);
;                 ssum += __builtin_bit_cast(float, __builtin_amdgcn_readlane(__builtin_bit_cast(int, score), selL));
;                 if (lane == selL) { r = kk; v = -__builtin_inff(); }
	s_nop 1
	v_max_f32_dpp v149, v149, v149 row_bcast:15 row_mask:0xa bank_mask:0xf
	s_nop 1
	v_max_f32_dpp v149, v149, v149 row_bcast:31 row_mask:0xc bank_mask:0xf
	s_nop 0
	v_readlane_b32 s22, v149, 63
	s_nop 1
	v_cmp_eq_f32_e32 vcc, s22, v147
	s_ff1_i32_b64 s22, vcc
	v_cmp_eq_u32_e32 vcc, s22, v163
	v_readlane_b32 s61, v146, s22
	s_nop 0
	v_cndmask_b32_e32 v147, v147, v211, vcc
	v_max_f32_e32 v150, v147, v147
	v_cndmask_b32_e64 v148, v148, 5, vcc
	v_max_f32_dpp v149, v147, v150 quad_perm:[1,0,3,2] row_mask:0xf bank_mask:0xf bound_ctrl:1


; template <int CTRL> __device__ __forceinline__ float dppf(float x) { return __builtin_bit_cast(float, __builtin_amdgcn_update_dpp(0, __builtin_bit_cast(int, x), CTRL, 0xF, 0xF, true)); }
; __device__ __forceinline__ void p9_fused4(Frame& F) {
;     ...
;                 float m = v; m = fmaxf(m, dppf<0xB1>(m)); m = fmaxf(m, dppf<0x4E>(m)); m = fmaxf(m, dppf<0x141>(m)); m = fmaxf(m, dppf<0x140>(m));
	s_nop 1
	v_max_f32_dpp v149, v149, v149 quad_perm:[2,3,0,1] row_mask:0xf bank_mask:0xf bound_ctrl:1


; template <int CTRL> __device__ __forceinline__ float dppf(float x) { return __builtin_bit_cast(float, __builtin_amdgcn_update_dpp(0, __builtin_bit_cast(int, x), CTRL, 0xF, 0xF, true)); }
; __device__ __forceinline__ void p9_fused4(Frame& F) {
;     ...
;                 float m = v; m = fmaxf(m, dppf<0xB1>(m)); m = fmaxf(m, dppf<0x4E>(m)); m = fmaxf(m, dppf<0x141>(m)); m = fmaxf(m, dppf<0x140>(m));
	s_nop 1
	v_max_f32_dpp v149, v149, v149 row_half_mirror row_mask:0xf bank_mask:0xf bound_ctrl:1


; template <int CTRL> __device__ __forceinline__ float dppf(float x) { return __builtin_bit_cast(float, __builtin_amdgcn_update_dpp(0, __builtin_bit_cast(int, x), CTRL, 0xF, 0xF, true)); }
; __device__ __forceinline__ void p9_fused4(Frame& F) {
;     ...
;                 float m = v; m = fmaxf(m, dppf<0xB1>(m)); m = fmaxf(m, dppf<0x4E>(m)); m = fmaxf(m, dppf<0x141>(m)); m = fmaxf(m, dppf<0x140>(m));
	s_nop 1
	v_max_f32_dpp v149, v149, v149 row_mirror row_mask:0xf bank_mask:0xf bound_ctrl:1


; template <int CTRL> __device__ __forceinline__ float dppf(float x) { return __builtin_bit_cast(float, __builtin_amdgcn_update_dpp(0, __builtin_bit_cast(int, x), CTRL, 0xF, 0xF, true)); }
; __device__ __forceinline__ void p9_fused4(Frame& F) {
;     ...
;                 float m = v; m = fmaxf(m, dppf<0xB1>(m)); m = fmaxf(m, dppf<0x4E>(m)); m = fmaxf(m, dppf<0x141>(m)); m = fmaxf(m, dppf<0x140>(m));
;                 const float r0 = __builtin_bit_cast(float, __builtin_amdgcn_readlane(__builtin_bit_cast(int, m), 0)), r1 = __builtin_bit_cast(float, __builtin_amdgcn_readlane(__builtin_bit_cast(int, m), 16));
;                 const float r2 = __builtin_bit_cast(float, __builtin_amdgcn_readlane(__builtin_bit_cast(int, m), 32)), r3 = __builtin_bit_cast(float, __builtin_amdgcn_readlane(__builtin_bit_cast(int, m), 48));
;                 const float wm = fmaxf(fmaxf(r0, r1), fmaxf(r2, r3));
;                 const unsigned long long bal = __builtin_amdgcn_ballot_w64(v == wm);
;                 const int selL = (int)__builtin_ctzll(bal);
;                 ssum += __builtin_bit_cast(float, __builtin_amdgcn_readlane(__builtin_bit_cast(int, score), selL));
;                 if (lane == selL) { r = kk; v = -__builtin_inff(); }
	s_nop 1
	v_max_f32_dpp v149, v149, v149 row_bcast:15 row_mask:0xa bank_mask:0xf
	s_nop 1
	v_max_f32_dpp v149, v149, v149 row_bcast:31 row_mask:0xc bank_mask:0xf
	s_nop 0
	v_readlane_b32 s22, v149, 63
	s_nop 1
	v_cmp_eq_f32_e32 vcc, s22, v147
	s_ff1_i32_b64 s22, vcc
	v_cmp_eq_u32_e32 vcc, s22, v163
	v_readlane_b32 s62, v146, s22
	s_nop 0
	v_cndmask_b32_e32 v147, v147, v211, vcc
	v_max_f32_e32 v150, v147, v147
	v_cndmask_b32_e64 v148, v148, 6, vcc
	v_max_f32_dpp v149, v147, v150 quad_perm:[1,0,3,2] row_mask:0xf bank_mask:0xf bound_ctrl:1


; template <int CTRL> __device__ __forceinline__ float dppf(float x) { return __builtin_bit_cast(float, __builtin_amdgcn_update_dpp(0, __builtin_bit_cast(int, x), CTRL, 0xF, 0xF, true)); }
; __device__ __forceinline__ void p9_fused4(Frame& F) {
;     ...
;                 float m = v; m = fmaxf(m, dppf<0xB1>(m)); m = fmaxf(m, dppf<0x4E>(m)); m = fmaxf(m, dppf<0x141>(m)); m = fmaxf(m, dppf<0x140>(m));
	s_nop 1
	v_max_f32_dpp v149, v149, v149 quad_perm:[2,3,0,1] row_mask:0xf bank_mask:0xf bound_ctrl:1


; template <int CTRL> __device__ __forceinline__ float dppf(float x) { return __builtin_bit_cast(float, __builtin_amdgcn_update_dpp(0, __builtin_bit_cast(int, x), CTRL, 0xF, 0xF, true)); }
; __device__ __forceinline__ void p9_fused4(Frame& F) {
;     ...
;                 float m = v; m = fmaxf(m, dppf<0xB1>(m)); m = fmaxf(m, dppf<0x4E>(m)); m = fmaxf(m, dppf<0x141>(m)); m = fmaxf(m, dppf<0x140>(m));
	s_nop 1
	v_max_f32_dpp v149, v149, v149 row_half_mirror row_mask:0xf bank_mask:0xf bound_ctrl:1


; template <int CTRL> __device__ __forceinline__ float dppf(float x) { return __builtin_bit_cast(float, __builtin_amdgcn_update_dpp(0, __builtin_bit_cast(int, x), CTRL, 0xF, 0xF, true)); }
; __device__ __forceinline__ void p9_fused4(Frame& F) {
;     ...
;                 float m = v; m = fmaxf(m, dppf<0xB1>(m)); m = fmaxf(m, dppf<0x4E>(m)); m = fmaxf(m, dppf<0x141>(m)); m = fmaxf(m, dppf<0x140>(m));
	s_nop 1
	v_max_f32_dpp v149, v149, v149 row_mirror row_mask:0xf bank_mask:0xf bound_ctrl:1


; template <int CTRL> __device__ __forceinline__ float dppf(float x) { return __builtin_bit_cast(float, __builtin_amdgcn_update_dpp(0, __builtin_bit_cast(int, x), CTRL, 0xF, 0xF, true)); }
; __device__ __forceinline__ void p9_fused4(Frame& F) {
;     ...
;             const float logit = lg[tl * 64 + lane];
;             const float score = 1.f / (1.f + __expf(-logit)), choice = score + rb;
;             float m1 = choice; m1 = fmaxf(m1, dppf<0xB1>(m1)); m1 = fmaxf(m1, dppf<0x4E>(m1)); m1 = fmaxf(m1, dppf<0x141>(m1));
;     ...
;                 if (lane == selL) { r = kk; v = -__builtin_inff(); }
;             }
;             const bool sel = r < 8;
;             if (sel) { WSP(int, WS_EIDX)[(size_t)t * 8 + r] = lane; WSP(float, WS_EW)[(size_t)t * 8 + r] = score / ssum * 2.5f; if (rp_ == 0) atomicAdd((int*)&hist[lane], 1); }
	s_nop 1
	v_max_f32_dpp v149, v149, v149 row_bcast:15 row_mask:0xa bank_mask:0xf
	s_nop 1
	v_max_f32_dpp v149, v149, v149 row_bcast:31 row_mask:0xc bank_mask:0xf
	s_nop 0
	v_readlane_b32 s22, v149, 63
	s_nop 1
	v_cmp_eq_f32_e32 vcc, s22, v147
	s_ff1_i32_b64 s22, vcc
	v_cmp_ne_u32_e32 vcc, s22, v163
	v_readlane_b32 s63, v146, s22
	s_nop 0
	v_cndmask_b32_e32 v164, 7, v148, vcc
	v_cmp_gt_u32_e32 vcc, 8, v164
	s_and_saveexec_b64 s[22:23], vcc
	s_cbranch_execz .LBB0_1407
	v_add_f32_e64 v147, s56, 0
	v_add_f32_e32 v147, s57, v147
	v_add_f32_e32 v147, s58, v147
	v_add_f32_e32 v147, s59, v147
	v_add_f32_e32 v147, s60, v147
	v_add_f32_e32 v147, s61, v147
	v_add_f32_e32 v147, s62, v147
	v_add_f32_e32 v147, s63, v147
	v_div_scale_f32 v152, s[56:57], v147, v147, v146
	v_rcp_f32_e32 v153, v152
	s_lshl_b64 s[24:25], s[24:25], 5
	v_lshlrev_b64 v[148:149], 2, v[164:165]
	v_or_b32_e32 v149, s25, v149
	v_or_b32_e32 v148, s24, v148
	v_lshl_add_u64 v[150:151], s[46:47], 0, v[148:149]
	global_store_dword v[150:151], v163, off
	v_fma_f32 v150, -v152, v153, 1.0
	v_fmac_f32_e32 v153, v150, v153
	v_div_scale_f32 v150, vcc, v146, v147, v146
	v_mul_f32_e32 v151, v150, v153
	v_fma_f32 v154, -v152, v151, v150
	v_fmac_f32_e32 v151, v154, v153
	v_fma_f32 v150, -v152, v151, v150
	v_div_fmas_f32 v150, v150, v153, v151
	v_div_fixup_f32 v146, v150, v147, v146
	v_mul_f32_e32 v150, 0x40200000, v146
	v_lshl_add_u64 v[146:147], s[48:49], 0, v[148:149]
	global_store_dword v[146:147], v150, off
	ds_add_u32 v193, v209
.LBB0_1407:
	s_or_b64 exec, exec, s[22:23]
	v_add_u32_e32 v146, s41, v191
	ds_read_b32 v146, v146
	s_waitcnt lgkmcnt(0)
	v_mul_f32_e32 v146, 0xbfb8aa3b, v146
	v_exp_f32_e32 v146, v146
	s_nop 0
	v_add_f32_e32 v146, 1.0, v146
	v_div_scale_f32 v147, s[22:23], v146, v146, 1.0
	v_rcp_f32_e32 v148, v147
	v_div_scale_f32 v149, vcc, 1.0, v146, 1.0
	v_fma_f32 v150, -v147, v148, 1.0
	v_fmac_f32_e32 v148, v150, v148
	v_mul_f32_e32 v150, v149, v148
	v_fma_f32 v151, -v147, v150, v149
	v_fmac_f32_e32 v150, v151, v148
	v_fma_f32 v147, -v147, v150, v149
	v_div_fmas_f32 v147, v147, v148, v150
	v_div_fixup_f32 v146, v147, v146, 1.0
	v_add_f32_e32 v147, v182, v146
	s_nop 1
	v_max_f32_dpp v148, v147, v147 quad_perm:[1,0,3,2] row_mask:0xf bank_mask:0xf bound_ctrl:1


; template <int CTRL> __device__ __forceinline__ float dppf(float x) { return __builtin_bit_cast(float, __builtin_amdgcn_update_dpp(0, __builtin_bit_cast(int, x), CTRL, 0xF, 0xF, true)); }
; __device__ __forceinline__ void p9_fused4(Frame& F) {
;     ...
;             float m1 = choice; m1 = fmaxf(m1, dppf<0xB1>(m1)); m1 = fmaxf(m1, dppf<0x4E>(m1)); m1 = fmaxf(m1, dppf<0x141>(m1));
	s_nop 1
	v_max_f32_dpp v148, v148, v148 quad_perm:[2,3,0,1] row_mask:0xf bank_mask:0xf bound_ctrl:1


; template <int CTRL> __device__ __forceinline__ float dppf(float x) { return __builtin_bit_cast(float, __builtin_amdgcn_update_dpp(0, __builtin_bit_cast(int, x), CTRL, 0xF, 0xF, true)); }
; __device__ __forceinline__ void p9_fused4(Frame& F) {
;     ...
;             float m1 = choice; m1 = fmaxf(m1, dppf<0xB1>(m1)); m1 = fmaxf(m1, dppf<0x4E>(m1)); m1 = fmaxf(m1, dppf<0x141>(m1));
	s_nop 1
	v_max_f32_dpp v148, v148, v148 row_half_mirror row_mask:0xf bank_mask:0xf bound_ctrl:1


; template <int CTRL> __device__ __forceinline__ float dppf(float x) { return __builtin_bit_cast(float, __builtin_amdgcn_update_dpp(0, __builtin_bit_cast(int, x), CTRL, 0xF, 0xF, true)); }
; template <int CTRL> __device__ __forceinline__ int dppi(int x) { return __builtin_amdgcn_update_dpp(0, x, CTRL, 0xF, 0xF, true); }
; __device__ __forceinline__ void p9_fused4(Frame& F) {
;     ...
;             int cand = (choice == m1) ? (lane & 7) : 8; cand = min(cand, dppi<0xB1>(cand)); cand = min(cand, dppi<0x4E>(cand)); cand = min(cand, dppi<0x141>(cand));
;             float m2 = ((lane & 7) == cand) ? -__builtin_inff() : choice; m2 = fmaxf(m2, dppf<0xB1>(m2)); m2 = fmaxf(m2, dppf<0x4E>(m2)); m2 = fmaxf(m2, dppf<0x141>(m2));
	v_cmp_eq_f32_e32 vcc, v147, v148
	s_nop 1
	v_cndmask_b32_e32 v149, 8, v192, vcc
	s_nop 1
	v_min_i32_dpp v149, v149, v149 quad_perm:[1,0,3,2] row_mask:0xf bank_mask:0xf bound_ctrl:1
	s_nop 1
	v_min_i32_dpp v149, v149, v149 quad_perm:[2,3,0,1] row_mask:0xf bank_mask:0xf bound_ctrl:1
	s_nop 1
	v_min_i32_dpp v149, v149, v149 row_half_mirror row_mask:0xf bank_mask:0xf bound_ctrl:1
	v_cmp_ne_u32_e32 vcc, v192, v149
	s_nop 1
	v_cndmask_b32_e32 v149, v211, v147, vcc
	s_nop 1
	v_max_f32_dpp v149, v149, v149 quad_perm:[1,0,3,2] row_mask:0xf bank_mask:0xf bound_ctrl:1


; template <int CTRL> __device__ __forceinline__ float dppf(float x) { return __builtin_bit_cast(float, __builtin_amdgcn_update_dpp(0, __builtin_bit_cast(int, x), CTRL, 0xF, 0xF, true)); }
; __device__ __forceinline__ void p9_fused4(Frame& F) {
;     ...
;             float m2 = ((lane & 7) == cand) ? -__builtin_inff() : choice; m2 = fmaxf(m2, dppf<0xB1>(m2)); m2 = fmaxf(m2, dppf<0x4E>(m2)); m2 = fmaxf(m2, dppf<0x141>(m2));
	s_nop 1
	v_max_f32_dpp v149, v149, v149 quad_perm:[2,3,0,1] row_mask:0xf bank_mask:0xf bound_ctrl:1


; template <int CTRL> __device__ __forceinline__ float dppf(float x) { return __builtin_bit_cast(float, __builtin_amdgcn_update_dpp(0, __builtin_bit_cast(int, x), CTRL, 0xF, 0xF, true)); }
; __device__ __forceinline__ void p9_fused4(Frame& F) {
;     ...
;             float m2 = ((lane & 7) == cand) ? -__builtin_inff() : choice; m2 = fmaxf(m2, dppf<0xB1>(m2)); m2 = fmaxf(m2, dppf<0x4E>(m2)); m2 = fmaxf(m2, dppf<0x141>(m2));
	s_nop 1
	v_max_f32_dpp v149, v149, v149 row_half_mirror row_mask:0xf bank_mask:0xf bound_ctrl:1


; template <int CTRL> __device__ __forceinline__ float dppf(float x) { return __builtin_bit_cast(float, __builtin_amdgcn_update_dpp(0, __builtin_bit_cast(int, x), CTRL, 0xF, 0xF, true)); }
; __device__ __forceinline__ void p9_fused4(Frame& F) {
;     ...
;             const float gs = m1 + m2; const int g = lane >> 3; int rank = 0;
; #pragma unroll
;             for (int gg = 0; gg < 8; ++gg) { const float sgg = __builtin_bit_cast(float, __builtin_amdgcn_readlane(__builtin_bit_cast(int, gs), gg * 8)); rank += (sgg > gs || (sgg == gs && gg < g)) ? 1 : 0; }
;             const float masked = (rank < 4) ? choice : -1e30f;
;             float v = masked, ssum = 0.f; int r = 8;
; #pragma unroll
;             for (int kk = 0; kk < 8; ++kk) {
;                 float m = v; m = fmaxf(m, dppf<0xB1>(m)); m = fmaxf(m, dppf<0x4E>(m)); m = fmaxf(m, dppf<0x141>(m)); m = fmaxf(m, dppf<0x140>(m));
	v_add_f32_e32 v148, v148, v149
	s_nop 0
	v_readlane_b32 s22, v148, 0
	v_readlane_b32 s56, v148, 8
	s_nop 0
	v_cmp_gt_f32_e32 vcc, s22, v148
	v_cmp_eq_f32_e64 s[22:23], s22, v148
	s_and_b64 s[22:23], s[22:23], s[6:7]
	s_or_b64 s[22:23], vcc, s[22:23]
	v_cmp_eq_f32_e32 vcc, s56, v148
	v_cmp_gt_f32_e64 s[24:25], s56, v148
	v_cndmask_b32_e64 v149, 0, 1, s[22:23]
	s_and_b64 s[22:23], vcc, s[8:9]
	s_or_b64 s[22:23], s[24:25], s[22:23]
	v_cndmask_b32_e64 v150, 0, 1, s[22:23]
	v_readlane_b32 s22, v148, 16
	s_nop 1
	v_cmp_gt_f32_e32 vcc, s22, v148
	v_cmp_eq_f32_e64 s[22:23], s22, v148
	s_and_b64 s[22:23], s[22:23], s[10:11]
	s_or_b64 s[22:23], vcc, s[22:23]
	v_cndmask_b32_e64 v151, 0, 1, s[22:23]
	v_readlane_b32 s22, v148, 24
	s_nop 1
	v_cmp_gt_f32_e32 vcc, s22, v148
	v_cmp_eq_f32_e64 s[22:23], s22, v148
	s_and_b64 s[22:23], s[22:23], s[12:13]
	s_or_b64 s[22:23], vcc, s[22:23]
	v_cndmask_b32_e64 v152, 0, 1, s[22:23]
	v_readlane_b32 s22, v148, 32
	s_nop 1
	v_cmp_gt_f32_e32 vcc, s22, v148
	v_cmp_eq_f32_e64 s[22:23], s22, v148
	s_and_b64 s[22:23], s[22:23], s[14:15]
	s_or_b64 s[22:23], vcc, s[22:23]
	v_cndmask_b32_e64 v153, 0, 1, s[22:23]
	v_readlane_b32 s22, v148, 40
	s_nop 1
	v_cmp_gt_f32_e32 vcc, s22, v148
	v_cmp_eq_f32_e64 s[22:23], s22, v148
	s_and_b64 s[22:23], s[22:23], s[16:17]
	s_or_b64 s[22:23], vcc, s[22:23]
	v_cndmask_b32_e64 v154, 0, 1, s[22:23]
	v_readlane_b32 s22, v148, 48
	s_nop 1
	v_cmp_gt_f32_e32 vcc, s22, v148
	v_cmp_eq_f32_e64 s[22:23], s22, v148
	s_and_b64 s[22:23], s[18:19], s[22:23]
	s_or_b64 s[22:23], vcc, s[22:23]
	v_cndmask_b32_e64 v155, 0, 1, s[22:23]
	v_readlane_b32 s22, v148, 56
	s_nop 1
	v_cmp_gt_f32_e32 vcc, s22, v148
	s_nop 1
	v_cndmask_b32_e64 v148, 0, 1, vcc
	v_add_u32_e32 v148, v150, v148
	v_add3_u32 v148, v148, v149, v151
	v_add3_u32 v148, v148, v152, v153
	v_add3_u32 v148, v148, v154, v155
	v_cmp_gt_u32_e32 vcc, 4, v148
	s_nop 1
	v_cndmask_b32_e32 v147, v212, v147, vcc
	s_nop 1
	v_max_f32_dpp v148, v147, v147 quad_perm:[1,0,3,2] row_mask:0xf bank_mask:0xf bound_ctrl:1


; template <int CTRL> __device__ __forceinline__ float dppf(float x) { return __builtin_bit_cast(float, __builtin_amdgcn_update_dpp(0, __builtin_bit_cast(int, x), CTRL, 0xF, 0xF, true)); }
; __device__ __forceinline__ void p9_fused4(Frame& F) {
;     ...
;                 float m = v; m = fmaxf(m, dppf<0xB1>(m)); m = fmaxf(m, dppf<0x4E>(m)); m = fmaxf(m, dppf<0x141>(m)); m = fmaxf(m, dppf<0x140>(m));
	s_nop 1
	v_max_f32_dpp v148, v148, v148 quad_perm:[2,3,0,1] row_mask:0xf bank_mask:0xf bound_ctrl:1


; template <int CTRL> __device__ __forceinline__ float dppf(float x) { return __builtin_bit_cast(float, __builtin_amdgcn_update_dpp(0, __builtin_bit_cast(int, x), CTRL, 0xF, 0xF, true)); }
; __device__ __forceinline__ void p9_fused4(Frame& F) {
;     ...
;                 float m = v; m = fmaxf(m, dppf<0xB1>(m)); m = fmaxf(m, dppf<0x4E>(m)); m = fmaxf(m, dppf<0x141>(m)); m = fmaxf(m, dppf<0x140>(m));
	s_nop 1
	v_max_f32_dpp v148, v148, v148 row_half_mirror row_mask:0xf bank_mask:0xf bound_ctrl:1


; template <int CTRL> __device__ __forceinline__ float dppf(float x) { return __builtin_bit_cast(float, __builtin_amdgcn_update_dpp(0, __builtin_bit_cast(int, x), CTRL, 0xF, 0xF, true)); }
; __device__ __forceinline__ void p9_fused4(Frame& F) {
;     ...
;                 float m = v; m = fmaxf(m, dppf<0xB1>(m)); m = fmaxf(m, dppf<0x4E>(m)); m = fmaxf(m, dppf<0x141>(m)); m = fmaxf(m, dppf<0x140>(m));
	s_nop 1
	v_max_f32_dpp v148, v148, v148 row_mirror row_mask:0xf bank_mask:0xf bound_ctrl:1


; template <int CTRL> __device__ __forceinline__ float dppf(float x) { return __builtin_bit_cast(float, __builtin_amdgcn_update_dpp(0, __builtin_bit_cast(int, x), CTRL, 0xF, 0xF, true)); }
; __device__ __forceinline__ void p9_fused4(Frame& F) {
;     ...
;                 float m = v; m = fmaxf(m, dppf<0xB1>(m)); m = fmaxf(m, dppf<0x4E>(m)); m = fmaxf(m, dppf<0x141>(m)); m = fmaxf(m, dppf<0x140>(m));
;                 const float r0 = __builtin_bit_cast(float, __builtin_amdgcn_readlane(__builtin_bit_cast(int, m), 0)), r1 = __builtin_bit_cast(float, __builtin_amdgcn_readlane(__builtin_bit_cast(int, m), 16));
;                 const float r2 = __builtin_bit_cast(float, __builtin_amdgcn_readlane(__builtin_bit_cast(int, m), 32)), r3 = __builtin_bit_cast(float, __builtin_amdgcn_readlane(__builtin_bit_cast(int, m), 48));
;                 const float wm = fmaxf(fmaxf(r0, r1), fmaxf(r2, r3));
;                 const unsigned long long bal = __builtin_amdgcn_ballot_w64(v == wm);
;                 const int selL = (int)__builtin_ctzll(bal);
;                 ssum += __builtin_bit_cast(float, __builtin_amdgcn_readlane(__builtin_bit_cast(int, score), selL));
;                 if (lane == selL) { r = kk; v = -__builtin_inff(); }
	s_nop 1
	v_max_f32_dpp v148, v148, v148 row_bcast:15 row_mask:0xa bank_mask:0xf
	s_nop 1
	v_max_f32_dpp v148, v148, v148 row_bcast:31 row_mask:0xc bank_mask:0xf
	s_nop 0
	v_readlane_b32 s22, v148, 63
	s_nop 1
	v_cmp_eq_f32_e32 vcc, s22, v147
	s_ff1_i32_b64 s22, vcc
	v_cmp_eq_u32_e32 vcc, s22, v163
	v_readlane_b32 s24, v146, s22
	s_nop 0
	v_cndmask_b32_e32 v147, v147, v211, vcc
	v_cndmask_b32_e64 v148, 8, 0, vcc
	s_nop 0
	v_max_f32_dpp v149, v147, v147 quad_perm:[1,0,3,2] row_mask:0xf bank_mask:0xf bound_ctrl:1


; template <int CTRL> __device__ __forceinline__ float dppf(float x) { return __builtin_bit_cast(float, __builtin_amdgcn_update_dpp(0, __builtin_bit_cast(int, x), CTRL, 0xF, 0xF, true)); }
; __device__ __forceinline__ void p9_fused4(Frame& F) {
;     ...
;                 float m = v; m = fmaxf(m, dppf<0xB1>(m)); m = fmaxf(m, dppf<0x4E>(m)); m = fmaxf(m, dppf<0x141>(m)); m = fmaxf(m, dppf<0x140>(m));
	s_nop 1
	v_max_f32_dpp v149, v149, v149 quad_perm:[2,3,0,1] row_mask:0xf bank_mask:0xf bound_ctrl:1


; template <int CTRL> __device__ __forceinline__ float dppf(float x) { return __builtin_bit_cast(float, __builtin_amdgcn_update_dpp(0, __builtin_bit_cast(int, x), CTRL, 0xF, 0xF, true)); }
; __device__ __forceinline__ void p9_fused4(Frame& F) {
;     ...
;                 float m = v; m = fmaxf(m, dppf<0xB1>(m)); m = fmaxf(m, dppf<0x4E>(m)); m = fmaxf(m, dppf<0x141>(m)); m = fmaxf(m, dppf<0x140>(m));
	s_nop 1
	v_max_f32_dpp v149, v149, v149 row_half_mirror row_mask:0xf bank_mask:0xf bound_ctrl:1


; template <int CTRL> __device__ __forceinline__ float dppf(float x) { return __builtin_bit_cast(float, __builtin_amdgcn_update_dpp(0, __builtin_bit_cast(int, x), CTRL, 0xF, 0xF, true)); }
; __device__ __forceinline__ void p9_fused4(Frame& F) {
;     ...
;                 float m = v; m = fmaxf(m, dppf<0xB1>(m)); m = fmaxf(m, dppf<0x4E>(m)); m = fmaxf(m, dppf<0x141>(m)); m = fmaxf(m, dppf<0x140>(m));
	s_nop 1
	v_max_f32_dpp v149, v149, v149 row_mirror row_mask:0xf bank_mask:0xf bound_ctrl:1


; template <int CTRL> __device__ __forceinline__ float dppf(float x) { return __builtin_bit_cast(float, __builtin_amdgcn_update_dpp(0, __builtin_bit_cast(int, x), CTRL, 0xF, 0xF, true)); }
; __device__ __forceinline__ void p9_fused4(Frame& F) {
;     ...
;                 float m = v; m = fmaxf(m, dppf<0xB1>(m)); m = fmaxf(m, dppf<0x4E>(m)); m = fmaxf(m, dppf<0x141>(m)); m = fmaxf(m, dppf<0x140>(m));
;                 const float r0 = __builtin_bit_cast(float, __builtin_amdgcn_readlane(__builtin_bit_cast(int, m), 0)), r1 = __builtin_bit_cast(float, __builtin_amdgcn_readlane(__builtin_bit_cast(int, m), 16));
;                 const float r2 = __builtin_bit_cast(float, __builtin_amdgcn_readlane(__builtin_bit_cast(int, m), 32)), r3 = __builtin_bit_cast(float, __builtin_amdgcn_readlane(__builtin_bit_cast(int, m), 48));
;                 const float wm = fmaxf(fmaxf(r0, r1), fmaxf(r2, r3));
;                 const unsigned long long bal = __builtin_amdgcn_ballot_w64(v == wm);
;                 const int selL = (int)__builtin_ctzll(bal);
;                 ssum += __builtin_bit_cast(float, __builtin_amdgcn_readlane(__builtin_bit_cast(int, score), selL));
;                 if (lane == selL) { r = kk; v = -__builtin_inff(); }
	s_nop 1
	v_max_f32_dpp v149, v149, v149 row_bcast:15 row_mask:0xa bank_mask:0xf
	s_nop 1
	v_max_f32_dpp v149, v149, v149 row_bcast:31 row_mask:0xc bank_mask:0xf
	s_nop 0
	v_readlane_b32 s22, v149, 63
	s_nop 1
	v_cmp_eq_f32_e32 vcc, s22, v147
	s_ff1_i32_b64 s22, vcc
	v_cmp_eq_u32_e32 vcc, s22, v163
	v_readlane_b32 s25, v146, s22
	s_nop 0
	v_cndmask_b32_e32 v147, v147, v211, vcc
	v_cndmask_b32_e64 v148, v148, 1, vcc
	s_nop 0
	v_max_f32_dpp v149, v147, v147 quad_perm:[1,0,3,2] row_mask:0xf bank_mask:0xf bound_ctrl:1


; template <int CTRL> __device__ __forceinline__ float dppf(float x) { return __builtin_bit_cast(float, __builtin_amdgcn_update_dpp(0, __builtin_bit_cast(int, x), CTRL, 0xF, 0xF, true)); }
; __device__ __forceinline__ void p9_fused4(Frame& F) {
;     ...
;                 float m = v; m = fmaxf(m, dppf<0xB1>(m)); m = fmaxf(m, dppf<0x4E>(m)); m = fmaxf(m, dppf<0x141>(m)); m = fmaxf(m, dppf<0x140>(m));
	s_nop 1
	v_max_f32_dpp v149, v149, v149 quad_perm:[2,3,0,1] row_mask:0xf bank_mask:0xf bound_ctrl:1


; template <int CTRL> __device__ __forceinline__ float dppf(float x) { return __builtin_bit_cast(float, __builtin_amdgcn_update_dpp(0, __builtin_bit_cast(int, x), CTRL, 0xF, 0xF, true)); }
; __device__ __forceinline__ void p9_fused4(Frame& F) {
;     ...
;                 float m = v; m = fmaxf(m, dppf<0xB1>(m)); m = fmaxf(m, dppf<0x4E>(m)); m = fmaxf(m, dppf<0x141>(m)); m = fmaxf(m, dppf<0x140>(m));
	s_nop 1
	v_max_f32_dpp v149, v149, v149 row_half_mirror row_mask:0xf bank_mask:0xf bound_ctrl:1


; template <int CTRL> __device__ __forceinline__ float dppf(float x) { return __builtin_bit_cast(float, __builtin_amdgcn_update_dpp(0, __builtin_bit_cast(int, x), CTRL, 0xF, 0xF, true)); }
; __device__ __forceinline__ void p9_fused4(Frame& F) {
;     ...
;                 float m = v; m = fmaxf(m, dppf<0xB1>(m)); m = fmaxf(m, dppf<0x4E>(m)); m = fmaxf(m, dppf<0x141>(m)); m = fmaxf(m, dppf<0x140>(m));
	s_nop 1
	v_max_f32_dpp v149, v149, v149 row_mirror row_mask:0xf bank_mask:0xf bound_ctrl:1


; template <int CTRL> __device__ __forceinline__ float dppf(float x) { return __builtin_bit_cast(float, __builtin_amdgcn_update_dpp(0, __builtin_bit_cast(int, x), CTRL, 0xF, 0xF, true)); }
; __device__ __forceinline__ void p9_fused4(Frame& F) {
;     ...
;                 float m = v; m = fmaxf(m, dppf<0xB1>(m)); m = fmaxf(m, dppf<0x4E>(m)); m = fmaxf(m, dppf<0x141>(m)); m = fmaxf(m, dppf<0x140>(m));
;                 const float r0 = __builtin_bit_cast(float, __builtin_amdgcn_readlane(__builtin_bit_cast(int, m), 0)), r1 = __builtin_bit_cast(float, __builtin_amdgcn_readlane(__builtin_bit_cast(int, m), 16));
;                 const float r2 = __builtin_bit_cast(float, __builtin_amdgcn_readlane(__builtin_bit_cast(int, m), 32)), r3 = __builtin_bit_cast(float, __builtin_amdgcn_readlane(__builtin_bit_cast(int, m), 48));
;                 const float wm = fmaxf(fmaxf(r0, r1), fmaxf(r2, r3));
;                 const unsigned long long bal = __builtin_amdgcn_ballot_w64(v == wm);
;                 const int selL = (int)__builtin_ctzll(bal);
;                 ssum += __builtin_bit_cast(float, __builtin_amdgcn_readlane(__builtin_bit_cast(int, score), selL));
;                 if (lane == selL) { r = kk; v = -__builtin_inff(); }
	s_nop 1
	v_max_f32_dpp v149, v149, v149 row_bcast:15 row_mask:0xa bank_mask:0xf
	s_nop 1
	v_max_f32_dpp v149, v149, v149 row_bcast:31 row_mask:0xc bank_mask:0xf
	s_nop 0
	v_readlane_b32 s22, v149, 63
	s_nop 1
	v_cmp_eq_f32_e32 vcc, s22, v147
	s_ff1_i32_b64 s22, vcc
	v_cmp_eq_u32_e32 vcc, s22, v163
	v_readlane_b32 s56, v146, s22
	s_nop 0
	v_cndmask_b32_e32 v147, v147, v211, vcc
	v_cndmask_b32_e64 v148, v148, 2, vcc
	s_nop 0
	v_max_f32_dpp v149, v147, v147 quad_perm:[1,0,3,2] row_mask:0xf bank_mask:0xf bound_ctrl:1


; template <int CTRL> __device__ __forceinline__ float dppf(float x) { return __builtin_bit_cast(float, __builtin_amdgcn_update_dpp(0, __builtin_bit_cast(int, x), CTRL, 0xF, 0xF, true)); }
; __device__ __forceinline__ void p9_fused4(Frame& F) {
;     ...
;                 float m = v; m = fmaxf(m, dppf<0xB1>(m)); m = fmaxf(m, dppf<0x4E>(m)); m = fmaxf(m, dppf<0x141>(m)); m = fmaxf(m, dppf<0x140>(m));
	s_nop 1
	v_max_f32_dpp v149, v149, v149 quad_perm:[2,3,0,1] row_mask:0xf bank_mask:0xf bound_ctrl:1


; template <int CTRL> __device__ __forceinline__ float dppf(float x) { return __builtin_bit_cast(float, __builtin_amdgcn_update_dpp(0, __builtin_bit_cast(int, x), CTRL, 0xF, 0xF, true)); }
; __device__ __forceinline__ void p9_fused4(Frame& F) {
;     ...
;                 float m = v; m = fmaxf(m, dppf<0xB1>(m)); m = fmaxf(m, dppf<0x4E>(m)); m = fmaxf(m, dppf<0x141>(m)); m = fmaxf(m, dppf<0x140>(m));
	s_nop 1
	v_max_f32_dpp v149, v149, v149 row_half_mirror row_mask:0xf bank_mask:0xf bound_ctrl:1


; template <int CTRL> __device__ __forceinline__ float dppf(float x) { return __builtin_bit_cast(float, __builtin_amdgcn_update_dpp(0, __builtin_bit_cast(int, x), CTRL, 0xF, 0xF, true)); }
; __device__ __forceinline__ void p9_fused4(Frame& F) {
;     ...
;                 float m = v; m = fmaxf(m, dppf<0xB1>(m)); m = fmaxf(m, dppf<0x4E>(m)); m = fmaxf(m, dppf<0x141>(m)); m = fmaxf(m, dppf<0x140>(m));
	s_nop 1
	v_max_f32_dpp v149, v149, v149 row_mirror row_mask:0xf bank_mask:0xf bound_ctrl:1


; template <int CTRL> __device__ __forceinline__ float dppf(float x) { return __builtin_bit_cast(float, __builtin_amdgcn_update_dpp(0, __builtin_bit_cast(int, x), CTRL, 0xF, 0xF, true)); }
; __device__ __forceinline__ void p9_fused4(Frame& F) {
;     ...
;                 float m = v; m = fmaxf(m, dppf<0xB1>(m)); m = fmaxf(m, dppf<0x4E>(m)); m = fmaxf(m, dppf<0x141>(m)); m = fmaxf(m, dppf<0x140>(m));
;                 const float r0 = __builtin_bit_cast(float, __builtin_amdgcn_readlane(__builtin_bit_cast(int, m), 0)), r1 = __builtin_bit_cast(float, __builtin_amdgcn_readlane(__builtin_bit_cast(int, m), 16));
;                 const float r2 = __builtin_bit_cast(float, __builtin_amdgcn_readlane(__builtin_bit_cast(int, m), 32)), r3 = __builtin_bit_cast(float, __builtin_amdgcn_readlane(__builtin_bit_cast(int, m), 48));
;                 const float wm = fmaxf(fmaxf(r0, r1), fmaxf(r2, r3));
;                 const unsigned long long bal = __builtin_amdgcn_ballot_w64(v == wm);
;                 const int selL = (int)__builtin_ctzll(bal);
;                 ssum += __builtin_bit_cast(float, __builtin_amdgcn_readlane(__builtin_bit_cast(int, score), selL));
;                 if (lane == selL) { r = kk; v = -__builtin_inff(); }
	s_nop 1
	v_max_f32_dpp v149, v149, v149 row_bcast:15 row_mask:0xa bank_mask:0xf
	s_nop 1
	v_max_f32_dpp v149, v149, v149 row_bcast:31 row_mask:0xc bank_mask:0xf
	s_nop 0
	v_readlane_b32 s22, v149, 63
	s_nop 1
	v_cmp_eq_f32_e32 vcc, s22, v147
	s_ff1_i32_b64 s22, vcc
	v_cmp_eq_u32_e32 vcc, s22, v163
	v_readlane_b32 s57, v146, s22
	s_nop 0
	v_cndmask_b32_e32 v147, v147, v211, vcc
	v_cndmask_b32_e64 v148, v148, 3, vcc
	s_nop 0
	v_max_f32_dpp v149, v147, v147 quad_perm:[1,0,3,2] row_mask:0xf bank_mask:0xf bound_ctrl:1


; template <int CTRL> __device__ __forceinline__ float dppf(float x) { return __builtin_bit_cast(float, __builtin_amdgcn_update_dpp(0, __builtin_bit_cast(int, x), CTRL, 0xF, 0xF, true)); }
; __device__ __forceinline__ void p9_fused4(Frame& F) {
;     ...
;                 float m = v; m = fmaxf(m, dppf<0xB1>(m)); m = fmaxf(m, dppf<0x4E>(m)); m = fmaxf(m, dppf<0x141>(m)); m = fmaxf(m, dppf<0x140>(m));
	s_nop 1
	v_max_f32_dpp v149, v149, v149 quad_perm:[2,3,0,1] row_mask:0xf bank_mask:0xf bound_ctrl:1


; template <int CTRL> __device__ __forceinline__ float dppf(float x) { return __builtin_bit_cast(float, __builtin_amdgcn_update_dpp(0, __builtin_bit_cast(int, x), CTRL, 0xF, 0xF, true)); }
; __device__ __forceinline__ void p9_fused4(Frame& F) {
;     ...
;                 float m = v; m = fmaxf(m, dppf<0xB1>(m)); m = fmaxf(m, dppf<0x4E>(m)); m = fmaxf(m, dppf<0x141>(m)); m = fmaxf(m, dppf<0x140>(m));
	s_nop 1
	v_max_f32_dpp v149, v149, v149 row_half_mirror row_mask:0xf bank_mask:0xf bound_ctrl:1


; template <int CTRL> __device__ __forceinline__ float dppf(float x) { return __builtin_bit_cast(float, __builtin_amdgcn_update_dpp(0, __builtin_bit_cast(int, x), CTRL, 0xF, 0xF, true)); }
; __device__ __forceinline__ void p9_fused4(Frame& F) {
;     ...
;                 float m = v; m = fmaxf(m, dppf<0xB1>(m)); m = fmaxf(m, dppf<0x4E>(m)); m = fmaxf(m, dppf<0x141>(m)); m = fmaxf(m, dppf<0x140>(m));
	s_nop 1
	v_max_f32_dpp v149, v149, v149 row_mirror row_mask:0xf bank_mask:0xf bound_ctrl:1


; template <int CTRL> __device__ __forceinline__ float dppf(float x) { return __builtin_bit_cast(float, __builtin_amdgcn_update_dpp(0, __builtin_bit_cast(int, x), CTRL, 0xF, 0xF, true)); }
; __device__ __forceinline__ void p9_fused4(Frame& F) {
;     ...
;                 float m = v; m = fmaxf(m, dppf<0xB1>(m)); m = fmaxf(m, dppf<0x4E>(m)); m = fmaxf(m, dppf<0x141>(m)); m = fmaxf(m, dppf<0x140>(m));
;                 const float r0 = __builtin_bit_cast(float, __builtin_amdgcn_readlane(__builtin_bit_cast(int, m), 0)), r1 = __builtin_bit_cast(float, __builtin_amdgcn_readlane(__builtin_bit_cast(int, m), 16));
;                 const float r2 = __builtin_bit_cast(float, __builtin_amdgcn_readlane(__builtin_bit_cast(int, m), 32)), r3 = __builtin_bit_cast(float, __builtin_amdgcn_readlane(__builtin_bit_cast(int, m), 48));
;                 const float wm = fmaxf(fmaxf(r0, r1), fmaxf(r2, r3));
;                 const unsigned long long bal = __builtin_amdgcn_ballot_w64(v == wm);
;                 const int selL = (int)__builtin_ctzll(bal);
;                 ssum += __builtin_bit_cast(float, __builtin_amdgcn_readlane(__builtin_bit_cast(int, score), selL));
;                 if (lane == selL) { r = kk; v = -__builtin_inff(); }
	s_nop 1
	v_max_f32_dpp v149, v149, v149 row_bcast:15 row_mask:0xa bank_mask:0xf
	s_nop 1
	v_max_f32_dpp v149, v149, v149 row_bcast:31 row_mask:0xc bank_mask:0xf
	s_nop 0
	v_readlane_b32 s22, v149, 63
	s_nop 1
	v_cmp_eq_f32_e32 vcc, s22, v147
	s_ff1_i32_b64 s22, vcc
	v_cmp_eq_u32_e32 vcc, s22, v163
	v_readlane_b32 s58, v146, s22
	s_nop 0
	v_cndmask_b32_e32 v147, v147, v211, vcc
	v_max_f32_e32 v150, v147, v147
	v_cndmask_b32_e64 v148, v148, 4, vcc
	v_max_f32_dpp v149, v147, v150 quad_perm:[1,0,3,2] row_mask:0xf bank_mask:0xf bound_ctrl:1


; template <int CTRL> __device__ __forceinline__ float dppf(float x) { return __builtin_bit_cast(float, __builtin_amdgcn_update_dpp(0, __builtin_bit_cast(int, x), CTRL, 0xF, 0xF, true)); }
; __device__ __forceinline__ void p9_fused4(Frame& F) {
;     ...
;                 float m = v; m = fmaxf(m, dppf<0xB1>(m)); m = fmaxf(m, dppf<0x4E>(m)); m = fmaxf(m, dppf<0x141>(m)); m = fmaxf(m, dppf<0x140>(m));
	s_nop 1
	v_max_f32_dpp v149, v149, v149 quad_perm:[2,3,0,1] row_mask:0xf bank_mask:0xf bound_ctrl:1


; template <int CTRL> __device__ __forceinline__ float dppf(float x) { return __builtin_bit_cast(float, __builtin_amdgcn_update_dpp(0, __builtin_bit_cast(int, x), CTRL, 0xF, 0xF, true)); }
; __device__ __forceinline__ void p9_fused4(Frame& F) {
;     ...
;                 float m = v; m = fmaxf(m, dppf<0xB1>(m)); m = fmaxf(m, dppf<0x4E>(m)); m = fmaxf(m, dppf<0x141>(m)); m = fmaxf(m, dppf<0x140>(m));
	s_nop 1
	v_max_f32_dpp v149, v149, v149 row_half_mirror row_mask:0xf bank_mask:0xf bound_ctrl:1


; template <int CTRL> __device__ __forceinline__ float dppf(float x) { return __builtin_bit_cast(float, __builtin_amdgcn_update_dpp(0, __builtin_bit_cast(int, x), CTRL, 0xF, 0xF, true)); }
; __device__ __forceinline__ void p9_fused4(Frame& F) {
;     ...
;                 float m = v; m = fmaxf(m, dppf<0xB1>(m)); m = fmaxf(m, dppf<0x4E>(m)); m = fmaxf(m, dppf<0x141>(m)); m = fmaxf(m, dppf<0x140>(m));
	s_nop 1
	v_max_f32_dpp v149, v149, v149 row_mirror row_mask:0xf bank_mask:0xf bound_ctrl:1


; template <int CTRL> __device__ __forceinline__ float dppf(float x) { return __builtin_bit_cast(float, __builtin_amdgcn_update_dpp(0, __builtin_bit_cast(int, x), CTRL, 0xF, 0xF, true)); }
; __device__ __forceinline__ void p9_fused4(Frame& F) {
;     ...
;                 float m = v; m = fmaxf(m, dppf<0xB1>(m)); m = fmaxf(m, dppf<0x4E>(m)); m = fmaxf(m, dppf<0x141>(m)); m = fmaxf(m, dppf<0x140>(m));
;                 const float r0 = __builtin_bit_cast(float, __builtin_amdgcn_readlane(__builtin_bit_cast(int, m), 0)), r1 = __builtin_bit_cast(float, __builtin_amdgcn_readlane(__builtin_bit_cast(int, m), 16));
;                 const float r2 = __builtin_bit_cast(float, __builtin_amdgcn_readlane(__builtin_bit_cast(int, m), 32)), r3 = __builtin_bit_cast(float, __builtin_amdgcn_readlane(__builtin_bit_cast(int, m), 48));
;                 const float wm = fmaxf(fmaxf(r0, r1), fmaxf(r2, r3));
;                 const unsigned long long bal = __builtin_amdgcn_ballot_w64(v == wm);
;                 const int selL = (int)__builtin_ctzll(bal);
;                 ssum += __builtin_bit_cast(float, __builtin_amdgcn_readlane(__builtin_bit_cast(int, score), selL));
;                 if (lane == selL) { r = kk; v = -__builtin_inff(); }
	s_nop 1
	v_max_f32_dpp v149, v149, v149 row_bcast:15 row_mask:0xa bank_mask:0xf
	s_nop 1
	v_max_f32_dpp v149, v149, v149 row_bcast:31 row_mask:0xc bank_mask:0xf
	s_nop 0
	v_readlane_b32 s22, v149, 63
	s_nop 1
	v_cmp_eq_f32_e32 vcc, s22, v147
	s_ff1_i32_b64 s22, vcc
	v_cmp_eq_u32_e32 vcc, s22, v163
	v_readlane_b32 s59, v146, s22
	s_nop 0
	v_cndmask_b32_e32 v147, v147, v211, vcc
	v_max_f32_e32 v150, v147, v147
	v_cndmask_b32_e64 v148, v148, 5, vcc
	v_max_f32_dpp v149, v147, v150 quad_perm:[1,0,3,2] row_mask:0xf bank_mask:0xf bound_ctrl:1


; template <int CTRL> __device__ __forceinline__ float dppf(float x) { return __builtin_bit_cast(float, __builtin_amdgcn_update_dpp(0, __builtin_bit_cast(int, x), CTRL, 0xF, 0xF, true)); }
; __device__ __forceinline__ void p9_fused4(Frame& F) {
;     ...
;                 float m = v; m = fmaxf(m, dppf<0xB1>(m)); m = fmaxf(m, dppf<0x4E>(m)); m = fmaxf(m, dppf<0x141>(m)); m = fmaxf(m, dppf<0x140>(m));
	s_nop 1
	v_max_f32_dpp v149, v149, v149 quad_perm:[2,3,0,1] row_mask:0xf bank_mask:0xf bound_ctrl:1


; template <int CTRL> __device__ __forceinline__ float dppf(float x) { return __builtin_bit_cast(float, __builtin_amdgcn_update_dpp(0, __builtin_bit_cast(int, x), CTRL, 0xF, 0xF, true)); }
; __device__ __forceinline__ void p9_fused4(Frame& F) {
;     ...
;                 float m = v; m = fmaxf(m, dppf<0xB1>(m)); m = fmaxf(m, dppf<0x4E>(m)); m = fmaxf(m, dppf<0x141>(m)); m = fmaxf(m, dppf<0x140>(m));
	s_nop 1
	v_max_f32_dpp v149, v149, v149 row_half_mirror row_mask:0xf bank_mask:0xf bound_ctrl:1


; template <int CTRL> __device__ __forceinline__ float dppf(float x) { return __builtin_bit_cast(float, __builtin_amdgcn_update_dpp(0, __builtin_bit_cast(int, x), CTRL, 0xF, 0xF, true)); }
; __device__ __forceinline__ void p9_fused4(Frame& F) {
;     ...
;                 float m = v; m = fmaxf(m, dppf<0xB1>(m)); m = fmaxf(m, dppf<0x4E>(m)); m = fmaxf(m, dppf<0x141>(m)); m = fmaxf(m, dppf<0x140>(m));
	s_nop 1
	v_max_f32_dpp v149, v149, v149 row_mirror row_mask:0xf bank_mask:0xf bound_ctrl:1


; template <int CTRL> __device__ __forceinline__ float dppf(float x) { return __builtin_bit_cast(float, __builtin_amdgcn_update_dpp(0, __builtin_bit_cast(int, x), CTRL, 0xF, 0xF, true)); }
; __device__ __forceinline__ void p9_fused4(Frame& F) {
;     ...
;                 float m = v; m = fmaxf(m, dppf<0xB1>(m)); m = fmaxf(m, dppf<0x4E>(m)); m = fmaxf(m, dppf<0x141>(m)); m = fmaxf(m, dppf<0x140>(m));
;                 const float r0 = __builtin_bit_cast(float, __builtin_amdgcn_readlane(__builtin_bit_cast(int, m), 0)), r1 = __builtin_bit_cast(float, __builtin_amdgcn_readlane(__builtin_bit_cast(int, m), 16));
;                 const float r2 = __builtin_bit_cast(float, __builtin_amdgcn_readlane(__builtin_bit_cast(int, m), 32)), r3 = __builtin_bit_cast(float, __builtin_amdgcn_readlane(__builtin_bit_cast(int, m), 48));
;                 const float wm = fmaxf(fmaxf(r0, r1), fmaxf(r2, r3));
;                 const unsigned long long bal = __builtin_amdgcn_ballot_w64(v == wm);
;                 const int selL = (int)__builtin_ctzll(bal);
;                 ssum += __builtin_bit_cast(float, __builtin_amdgcn_readlane(__builtin_bit_cast(int, score), selL));
;                 if (lane == selL) { r = kk; v = -__builtin_inff(); }
	s_nop 1
	v_max_f32_dpp v149, v149, v149 row_bcast:15 row_mask:0xa bank_mask:0xf
	s_nop 1
	v_max_f32_dpp v149, v149, v149 row_bcast:31 row_mask:0xc bank_mask:0xf
	s_nop 0
	v_readlane_b32 s22, v149, 63
	s_nop 1
	v_cmp_eq_f32_e32 vcc, s22, v147
	s_ff1_i32_b64 s22, vcc
	v_cmp_eq_u32_e32 vcc, s22, v163
	v_readlane_b32 s60, v146, s22
	s_nop 0
	v_cndmask_b32_e32 v147, v147, v211, vcc
	v_max_f32_e32 v150, v147, v147
	v_cndmask_b32_e64 v148, v148, 6, vcc
	v_max_f32_dpp v149, v147, v150 quad_perm:[1,0,3,2] row_mask:0xf bank_mask:0xf bound_ctrl:1


; template <int CTRL> __device__ __forceinline__ float dppf(float x) { return __builtin_bit_cast(float, __builtin_amdgcn_update_dpp(0, __builtin_bit_cast(int, x), CTRL, 0xF, 0xF, true)); }
; __device__ __forceinline__ void p9_fused4(Frame& F) {
;     ...
;                 float m = v; m = fmaxf(m, dppf<0xB1>(m)); m = fmaxf(m, dppf<0x4E>(m)); m = fmaxf(m, dppf<0x141>(m)); m = fmaxf(m, dppf<0x140>(m));
	s_nop 1
	v_max_f32_dpp v149, v149, v149 quad_perm:[2,3,0,1] row_mask:0xf bank_mask:0xf bound_ctrl:1


; template <int CTRL> __device__ __forceinline__ float dppf(float x) { return __builtin_bit_cast(float, __builtin_amdgcn_update_dpp(0, __builtin_bit_cast(int, x), CTRL, 0xF, 0xF, true)); }
; __device__ __forceinline__ void p9_fused4(Frame& F) {
;     ...
;                 float m = v; m = fmaxf(m, dppf<0xB1>(m)); m = fmaxf(m, dppf<0x4E>(m)); m = fmaxf(m, dppf<0x141>(m)); m = fmaxf(m, dppf<0x140>(m));
	s_nop 1
	v_max_f32_dpp v149, v149, v149 row_half_mirror row_mask:0xf bank_mask:0xf bound_ctrl:1


; template <int CTRL> __device__ __forceinline__ float dppf(float x) { return __builtin_bit_cast(float, __builtin_amdgcn_update_dpp(0, __builtin_bit_cast(int, x), CTRL, 0xF, 0xF, true)); }
; __device__ __forceinline__ void p9_fused4(Frame& F) {
;     ...
;                 float m = v; m = fmaxf(m, dppf<0xB1>(m)); m = fmaxf(m, dppf<0x4E>(m)); m = fmaxf(m, dppf<0x141>(m)); m = fmaxf(m, dppf<0x140>(m));
	s_nop 1
	v_max_f32_dpp v149, v149, v149 row_mirror row_mask:0xf bank_mask:0xf bound_ctrl:1


; template <int CTRL> __device__ __forceinline__ float dppf(float x) { return __builtin_bit_cast(float, __builtin_amdgcn_update_dpp(0, __builtin_bit_cast(int, x), CTRL, 0xF, 0xF, true)); }
; __device__ __forceinline__ void p9_fused4(Frame& F) {
;     ...
;                 float m = v; m = fmaxf(m, dppf<0xB1>(m)); m = fmaxf(m, dppf<0x4E>(m)); m = fmaxf(m, dppf<0x141>(m)); m = fmaxf(m, dppf<0x140>(m));
;                 const float r0 = __builtin_bit_cast(float, __builtin_amdgcn_readlane(__builtin_bit_cast(int, m), 0)), r1 = __builtin_bit_cast(float, __builtin_amdgcn_readlane(__builtin_bit_cast(int, m), 16));
;                 const float r2 = __builtin_bit_cast(float, __builtin_amdgcn_readlane(__builtin_bit_cast(int, m), 32)), r3 = __builtin_bit_cast(float, __builtin_amdgcn_readlane(__builtin_bit_cast(int, m), 48));
;                 const float wm = fmaxf(fmaxf(r0, r1), fmaxf(r2, r3));
;                 const unsigned long long bal = __builtin_amdgcn_ballot_w64(v == wm);
;                 const int selL = (int)__builtin_ctzll(bal);
;                 ssum += __builtin_bit_cast(float, __builtin_amdgcn_readlane(__builtin_bit_cast(int, score), selL));
;                 if (lane == selL) { r = kk; v = -__builtin_inff(); }
;             }
;             const bool sel = r < 8;
;             if (sel) { WSP(int, WS_EIDX)[(size_t)t * 8 + r] = lane; WSP(float, WS_EW)[(size_t)t * 8 + r] = score / ssum * 2.5f; if (rp_ == 0) atomicAdd((int*)&hist[lane], 1); }
	s_nop 1
	v_max_f32_dpp v149, v149, v149 row_bcast:15 row_mask:0xa bank_mask:0xf
	s_nop 1
	v_max_f32_dpp v149, v149, v149 row_bcast:31 row_mask:0xc bank_mask:0xf
	s_nop 0
	v_readlane_b32 s22, v149, 63
	s_nop 1
	v_cmp_eq_f32_e32 vcc, s22, v147
	s_ff1_i32_b64 s22, vcc
	v_cmp_ne_u32_e32 vcc, s22, v163
	v_readlane_b32 s61, v146, s22
	s_nop 0
	v_cndmask_b32_e32 v164, 7, v148, vcc
	v_cmp_gt_u32_e32 vcc, 8, v164
	s_and_saveexec_b64 s[22:23], vcc
	s_cbranch_execz .LBB0_1398
	v_add_f32_e64 v147, s24, 0
	v_add_f32_e32 v147, s25, v147
	v_add_f32_e32 v147, s56, v147
	v_add_f32_e32 v147, s57, v147
	v_add_f32_e32 v147, s58, v147
	v_add_f32_e32 v147, s59, v147
	v_add_f32_e32 v147, s60, v147
	v_add_f32_e32 v147, s61, v147
	s_lshl_b64 s[24:25], s[50:51], 5
	v_div_scale_f32 v152, s[50:51], v147, v147, v146
	v_rcp_f32_e32 v153, v152
	v_lshlrev_b64 v[148:149], 2, v[164:165]
	v_or_b32_e32 v149, s25, v149
	v_or_b32_e32 v148, s24, v148
	v_lshl_add_u64 v[150:151], s[46:47], 0, v[148:149]
	global_store_dword v[150:151], v163, off
	v_fma_f32 v150, -v152, v153, 1.0
	v_fmac_f32_e32 v153, v150, v153
	v_div_scale_f32 v150, vcc, v146, v147, v146
	v_mul_f32_e32 v151, v150, v153
	v_fma_f32 v154, -v152, v151, v150
	v_fmac_f32_e32 v151, v154, v153
	v_fma_f32 v150, -v152, v151, v150
	v_div_fmas_f32 v150, v150, v153, v151
	v_div_fixup_f32 v146, v150, v147, v146
	v_mul_f32_e32 v150, 0x40200000, v146
	v_lshl_add_u64 v[146:147], s[48:49], 0, v[148:149]
	global_store_dword v[146:147], v150, off
	ds_add_u32 v193, v209
	s_branch .LBB0_1398
